# speedup vs baseline: 1.0090x; 1.0090x over previous
.Lrp_skip:
	s_or_b64 exec, exec, s[42:43]
	s_movk_i32 s8, 0x100
	v_cmp_gt_u32_e64 s[50:51], s8, v0
	s_and_saveexec_b64 s[8:9], s[50:51]
	v_mov_b32_e32 v4, 0x21e00
	v_lshl_add_u32 v4, v0, 2, v4
	v_mov_b32_e32 v5, 0
	ds_write_b32 v4, v5
	s_or_b64 exec, exec, s[8:9]
	v_cmp_eq_u32_e32 vcc, 0, v0
	s_and_saveexec_b64 s[8:9], vcc
	v_mov_b32_e32 v4, 0
	v_mov_b32_e32 v5, 0x22c50
	ds_write_b32 v5, v4
	s_or_b64 exec, exec, s[8:9]
	v_and_b32_e32 v18, 63, v0
	v_lshlrev_b32_e32 v4, 3, v18
	global_load_dwordx2 v[12:13], v4, s[44:45] offset:1024
	global_load_dwordx2 v[6:7], v4, s[44:45] offset:1536
	global_load_dwordx2 v[14:15], v4, s[44:45]
	global_load_dwordx2 v[16:17], v4, s[46:47]
	global_load_dwordx2 v[8:9], v4, s[44:45] offset:512
	global_load_dwordx2 v[10:11], v4, s[46:47] offset:512
	s_mov_b64 s[68:69], s[44:45]
	s_mov_b64 s[70:71], s[46:47]
	s_movk_i32 s48, 0x1c0
	v_cmp_gt_u32_e32 vcc, s48, v0
	v_mov_b32_e32 v62, 223
	v_mov_b32_e32 v63, 0x24160
	v_cndmask_b32_e32 v62, 0, v62, vcc
	v_lshl_add_u32 v63, v0, 2, v63
	s_movk_i32 s48, 0x1c2
	v_cmp_gt_u32_e32 vcc, s48, v0
	s_and_saveexec_b64 s[48:49], vcc
	ds_write_b32 v63, v62
	s_or_b64 exec, exec, s[48:49]
	s_waitcnt lgkmcnt(0)
	s_sub_i32 s25, s39, s38
	v_mov_b32_e32 v20, s38
	v_or_b32_e32 v23, 0x400, v0
	v_or_b32_e32 v22, 0x800, v0
	v_or_b32_e32 v21, 0xc00, v0
	v_cmp_gt_i32_e32 vcc, s25, v0
	v_cmp_gt_i32_e64 s[6:7], s25, v23
	v_cmp_gt_i32_e64 s[8:9], s25, v22
	v_cndmask_b32_e32 v27, 0, v0, vcc
	v_add_u32_e32 v2, v27, v20
	v_cndmask_b32_e64 v27, 0, v23, s[6:7]
	v_add_u32_e32 v4, v27, v20
	v_cndmask_b32_e64 v27, 0, v22, s[8:9]
	v_add_u32_e32 v24, v27, v20
	v_cmp_gt_i32_e64 s[10:11], s25, v21
	v_ashrrev_i32_e32 v25, 31, v24
	v_ashrrev_i32_e32 v3, 31, v2
	v_cndmask_b32_e64 v27, 0, v21, s[10:11]
	v_lshl_add_u64 v[30:31], v[24:25], 2, s[18:19]
	v_add_u32_e32 v24, v27, v20
	v_lshl_add_u64 v[2:3], v[2:3], 2, s[18:19]
	v_ashrrev_i32_e32 v5, 31, v4
	v_ashrrev_i32_e32 v25, 31, v24
	v_lshl_add_u64 v[4:5], v[4:5], 2, s[18:19]
	v_lshl_add_u64 v[32:33], v[24:25], 2, s[18:19]
	global_load_dword v25, v[2:3], off
	global_load_dword v26, v[4:5], off
	global_load_dword v28, v[30:31], off
	global_load_dword v29, v[32:33], off
	s_and_saveexec_b64 s[42:43], s[40:41]
	s_cbranch_execz .Lrp_skip2
	v_mov_b32_e32 v2, 0x228a0
	v_lshl_add_u32 v2, v0, 2, v2
	s_waitcnt vmcnt(10)
	ds_write_b32 v2, v1

.LBB3_26:
	s_or_b64 exec, exec, s[12:13]
	s_waitcnt vmcnt(3)
	v_cndmask_b32_e32 v30, -1, v25, vcc
	v_and_b32_e32 v2, 0xffff, v30
	v_cmp_eq_u32_e32 vcc, -1, v30
	s_waitcnt vmcnt(2)
	v_cndmask_b32_e64 v27, -1, v26, s[6:7]
	v_cmp_eq_u32_e64 s[12:13], -1, v27
	v_cndmask_b32_e64 v2, v2, 0, vcc
	v_lshlrev_b32_e32 v25, 3, v2
	v_and_b32_e32 v2, 0xffff, v27
	s_waitcnt vmcnt(1)
	v_cndmask_b32_e64 v5, -1, v28, s[8:9]
	v_cndmask_b32_e64 v2, v2, 0, s[12:13]
	v_lshlrev_b32_e32 v26, 3, v2
	v_and_b32_e32 v2, 0xffff, v5
	v_cmp_eq_u32_e64 s[14:15], -1, v5
	s_waitcnt vmcnt(0)
	v_cndmask_b32_e64 v4, -1, v29, s[10:11]
	v_cmp_eq_u32_e64 s[16:17], -1, v4
	v_cndmask_b32_e64 v2, v2, 0, s[14:15]
	v_lshlrev_b32_e32 v31, 3, v2
	global_load_dwordx2 v[2:3], v25, s[20:21]
	global_load_dwordx2 v[28:29], v26, s[20:21]
	global_load_dwordx2 v[38:39], v31, s[20:21]
	v_and_b32_e32 v25, 0xffff, v4
	v_cndmask_b32_e64 v25, v25, 0, s[16:17]
	v_lshlrev_b32_e32 v25, 3, v25
	global_load_dwordx2 v[40:41], v25, s[20:21]
	v_and_b32_e32 v104, 31, v18
	v_lshlrev_b32_e32 v104, 2, v104
	global_load_dword v64, v104, s[68:69] offset:0
	global_load_dword v65, v104, s[68:69] offset:1024
	global_load_dword v66, v104, s[70:71] offset:0
	global_load_dword v68, v104, s[68:69] offset:128
	global_load_dword v69, v104, s[68:69] offset:1152
	global_load_dword v70, v104, s[70:71] offset:128
	global_load_dword v72, v104, s[68:69] offset:256
	global_load_dword v73, v104, s[68:69] offset:1280
	global_load_dword v74, v104, s[70:71] offset:256
	global_load_dword v76, v104, s[68:69] offset:384
	global_load_dword v77, v104, s[68:69] offset:1408
	global_load_dword v78, v104, s[70:71] offset:384
	global_load_dword v80, v104, s[68:69] offset:512
	global_load_dword v81, v104, s[68:69] offset:1536
	global_load_dword v82, v104, s[70:71] offset:512
	global_load_dword v84, v104, s[68:69] offset:640
	global_load_dword v85, v104, s[68:69] offset:1664
	global_load_dword v86, v104, s[70:71] offset:640
	global_load_dword v88, v104, s[68:69] offset:768
	global_load_dword v89, v104, s[68:69] offset:1792
	global_load_dword v90, v104, s[70:71] offset:768
	global_load_dword v92, v104, s[68:69] offset:896
	global_load_dword v93, v104, s[68:69] offset:1920
	global_load_dword v94, v104, s[70:71] offset:896
	s_and_b64 s[34:35], exec, s[28:29]
	s_cbranch_scc0 .Lt1a_skip
	v_and_b32_e32 v63, 31, v18
	v_lshrrev_b32_e32 v55, 3, v63
	v_lshlrev_b32_e32 v56, 2, v55
	v_and_b32_e32 v57, 3, v63
	v_add_u32_e32 v56, v56, v57
	v_lshlrev_b32_e32 v55, 4, v55
	v_bfe_u32 v57, v63, 1, 1
	v_lshl_add_u32 v55, v57, 3, v55
	v_and_b32_e32 v57, 1, v63
	v_cmp_eq_u32_e64 s[36:37], 1, v57
	v_mov_b32_e32 v57, 0x5040100
	v_mov_b32_e32 v103, 0x7060302
	v_lshlrev_b32_e32 v58, 1, v63
	v_cndmask_b32_e64 v57, v57, v103, s[36:37]
	v_cmp_gt_u32_e64 s[36:37], 32, v18
	v_mov_b32_e32 v59, 0x22c50
	v_mov_b32_e32 v60, 1
	v_mov_b32_e32 v62, 0x3c003c00
	v_cndmask_b32_e64 v63, 0, -1, s[36:37]
	v_mov_b32_e32 v61, 0x22c60
	s_mov_b32 s54, 0xf0f0f0f0
	s_mov_b32 s55, 0
	s_mov_b32 s56, 0
	s_mov_b32 s57, -1
	s_mov_b32 s64, 0x24160
	s_mov_b32 s65, 0x244e0
	s_movk_i32 s49, 0x210
	v_mov_b32_e32 v108, 0x24860
	v_mov_b32_e32 v109, 0x244e0
	v_mov_b32_e32 v110, 0x24160
	v_lshrrev_b32_e32 v98, 2, v0
	v_and_b32_e32 v99, 3, v0
	v_mov_b32_e32 v96, 0
	v_mov_b32_e32 v97, 0
	v_cmp_gt_u32_e64 s[36:37], s3, v98
	s_and_saveexec_b64 s[38:39], s[36:37]
	s_cbranch_execz .Lt1a_nr
	v_lshlrev_b32_e32 v103, 2, v98
	v_add_u32_e32 v104, 0x228a0, v103
	v_add_u32_e32 v105, 0x22580, v103
	ds_read2_b32 v[106:107], v104 offset1:1
	ds_read_b32 v97, v105
	s_waitcnt lgkmcnt(0)
	v_sub_u32_e32 v96, v107, v106
.Lt1a_nr:
	s_mov_b64 exec, s[38:39]
	v_cmp_eq_u32_e64 s[40:41], 0, v99
	s_movk_i32 s44, 0xe0
	v_cmp_gt_u32_e64 s[42:43], s44, v98
	v_add_u32_e32 v103, -1, v96
	v_ffbh_u32_e32 v103, v103
	s_and_b64 s[40:41], s[40:41], s[42:43]
	s_and_saveexec_b64 s[38:39], s[40:41]
	v_sub_u32_e32 v103, 32, v103
	v_cmp_lt_u32_e64 s[42:43], 1, v96
	v_lshlrev_b32_e32 v104, 4, v97
	v_add_u32_e32 v104, 0x1ce00, v104
	v_cndmask_b32_e64 v103, 0, v103, s[42:43]
	v_lshlrev_b32_e32 v101, 23, v103
	v_mov_b32_e32 v105, v96
	v_sub_u32_e32 v100, 0x46800000, v101
	v_lshlrev_b32_e32 v106, 3, v98
	v_add_u32_e32 v106, 0x22c60, v106
	ds_write_b64 v106, v[104:105]
	v_cmp_lt_u32_e64 s[46:47], 16, v96
	s_and_b64 s[44:45], exec, s[36:37]
	s_and_b64 s[40:41], s[44:45], s[46:47]
	s_andn2_b64 s[44:45], s[44:45], s[46:47]
	s_bcnt1_i32_b64 s42, s[40:41]
	s_bcnt1_i32_b64 s43, s[44:45]
	s_mov_b64 exec, 1
	v_mov_b32_e32 v106, s42
	v_mov_b32_e32 v107, s43
	ds_add_rtn_u32 v111, v108, v106
	ds_add_rtn_u32 v106, v108, v107 offset:4
	s_waitcnt lgkmcnt(0)
	v_readfirstlane_b32 s42, v111
	v_readfirstlane_b32 s43, v106
	s_mov_b64 exec, s[40:41]
	v_mbcnt_lo_u32_b32 v106, s40, 0
	v_mbcnt_hi_u32_b32 v106, s41, v106
	v_add_u32_e32 v106, s42, v106
	v_lshl_add_u32 v106, v106, 2, v110
	ds_write_b32 v106, v98
	s_mov_b64 exec, s[44:45]
	v_mbcnt_lo_u32_b32 v106, s44, 0
	v_mbcnt_hi_u32_b32 v106, s45, v106
	v_add_u32_e32 v106, s43, v106
	v_lshl_add_u32 v106, v106, 2, v109
	ds_write_b32 v106, v98
	s_mov_b64 exec, s[38:39]
.Lt1a_skip:
	v_or_b32_e32 v36, 0x1000, v0
	s_xor_b64 s[26:27], s[28:29], -1
	v_cmp_ne_u32_e64 s[10:11], -1, v30
	v_cmp_ne_u32_e64 s[8:9], -1, v27
	v_cmp_ne_u32_e64 s[0:1], -1, v5
	v_cmp_ne_u32_e64 s[6:7], -1, v4
	s_waitcnt vmcnt(27)
	v_cndmask_b32_e64 v34, v3, 0, vcc
	v_cndmask_b32_e64 v35, v2, 0, vcc
	s_waitcnt vmcnt(26)
	v_cndmask_b32_e64 v31, v29, 0, s[12:13]
	v_cndmask_b32_e64 v32, v28, 0, s[12:13]
	s_waitcnt vmcnt(25)
	v_cndmask_b32_e64 v28, v39, 0, s[14:15]
	v_cndmask_b32_e64 v29, v38, 0, s[14:15]
	s_waitcnt vmcnt(24)
	v_cndmask_b32_e64 v25, v41, 0, s[16:17]
	v_cndmask_b32_e64 v26, v40, 0, s[16:17]
	v_max3_f32 v2, v35, 0, v32
	v_max3_f32 v3, v34, 0, v31
	v_max3_f32 v38, v2, v29, v26
	v_max3_f32 v37, v3, v28, v25
	v_cmp_gt_i32_e32 vcc, s25, v36
	s_and_saveexec_b64 s[12:13], vcc
	s_cbranch_execz .LBB3_30
	v_add_u32_e32 v2, v0, v20
	v_add_u32_e32 v2, 0x1000, v2
	v_ashrrev_i32_e32 v3, 31, v2
	v_lshl_add_u64 v[2:3], v[2:3], 2, s[18:19]
	s_mov_b64 s[14:15], 0
	s_mov_b64 s[16:17], 0x1000
	v_mov_b32_e32 v39, 3

.LBB3_39:
	v_cvt_f16_f32_e32 v3, v14
	v_cvt_f16_f32_e32 v4, v12
	v_mul_f32_e32 v21, v16, v2
	v_fma_mixlo_f16 v5, v16, v2, 0
	v_mul_u32_u24_e32 v16, 0x10001, v3
	v_mul_u32_u24_e32 v22, 0x10001, v4
	v_cvt_f16_f32_e32 v3, v15
	v_cvt_f16_f32_e32 v4, v13
	s_mov_b32 s0, 0x10001
	v_mul_u32_u24_sdwa v23, v5, s0 dst_sel:DWORD dst_unused:UNUSED_PAD src0_sel:WORD_0 src1_sel:DWORD
	v_mul_f32_e32 v24, v17, v2
	v_fma_mixlo_f16 v5, v17, v2, 0
	v_mul_u32_u24_e32 v17, 0x10001, v3
	v_mul_u32_u24_e32 v25, 0x10001, v4
	v_cvt_f16_f32_e32 v3, v8
	v_cvt_f16_f32_e32 v4, v6
	v_mul_u32_u24_sdwa v26, v5, s0 dst_sel:DWORD dst_unused:UNUSED_PAD src0_sel:WORD_0 src1_sel:DWORD
	v_mul_f32_e32 v27, v10, v2
	v_fma_mixlo_f16 v5, v10, v2, 0
	v_mul_u32_u24_e32 v10, 0x10001, v3
	v_mul_u32_u24_e32 v28, 0x10001, v4
	v_cvt_f16_f32_e32 v3, v9
	v_cvt_f16_f32_e32 v4, v7
	v_sub_u32_e32 v20, 0x7f000000, v2
	v_mul_f32_e32 v14, v14, v2
	v_mul_f32_e32 v12, v12, v2
	v_mul_f32_e32 v15, v15, v2
	v_mul_f32_e32 v13, v13, v2
	v_mul_u32_u24_sdwa v29, v5, s0 dst_sel:DWORD dst_unused:UNUSED_PAD src0_sel:WORD_0 src1_sel:DWORD
	v_mul_f32_e32 v8, v8, v2
	v_mul_f32_e32 v6, v6, v2
	v_mul_f32_e32 v30, v11, v2
	v_fma_mixlo_f16 v5, v11, v2, 0
	v_mul_f32_e32 v9, v9, v2
	v_mul_f32_e32 v7, v7, v2
	v_cndmask_b32_e64 v2, 0, 1, s[26:27]
	v_mul_u32_u24_e32 v11, 0x10001, v3
	v_mul_u32_u24_e32 v31, 0x10001, v4
	v_mul_u32_u24_sdwa v32, v5, s0 dst_sel:DWORD dst_unused:UNUSED_PAD src0_sel:WORD_0 src1_sel:DWORD
	v_lshlrev_b32_e32 v33, 1, v33
	v_mov_b32_e32 v34, 0x22c50
	v_cmp_ne_u32_e64 s[6:7], 1, v2
	s_movk_i32 s12, 0x3c00
	v_mov_b32_e32 v35, 0x3c00
	s_sub_i32 s34, 0xe0, s3
	s_mul_i32 s35, s34, 33
	s_mul_i32 s36, s3, 0x210
	v_mov_b32_e32 v104, 0
	v_mov_b32_e32 v105, 0
	v_mov_b32_e32 v106, 0
	v_mov_b32_e32 v107, 0
	v_mov_b32_e32 v108, v0
	v_lshlrev_b32_e32 v109, 4, v0
	v_add_u32_e32 v109, s36, v109
	s_mov_b64 s[36:37], exec
.Lz_loop:
	v_cmp_gt_u32_e32 vcc, s35, v108
	s_and_b64 exec, exec, vcc
	s_cbranch_execz .Lz_done
	ds_write_b128 v109, v[104:107]
	v_add_u32_e32 v108, 0x400, v108
	v_add_u32_e32 v109, 0x4000, v109
	s_branch .Lz_loop
.Lz_done:
	s_mov_b64 exec, s[36:37]
	v_cmp_gt_u32_e32 vcc, s34, v0
	v_add_u32_e32 v109, s3, v0
	v_lshlrev_b32_e32 v109, 2, v109
	v_add_u32_e32 v109, 0x22200, v109
	s_and_saveexec_b64 s[36:37], vcc
	ds_write_b32 v109, v104
	s_mov_b64 exec, s[36:37]
	s_waitcnt lgkmcnt(0)
	s_barrier
	s_and_b64 vcc, exec, s[6:7]
	s_cbranch_vccz .LBB3_43
	v_sub_u32_e32 v103, 0x7f000000, v20
	s_waitcnt vmcnt(0)
	v_cvt_pk_f16_f32 v64, v64, v65
	v_mul_f32_e32 v66, v103, v66
	v_cvt_pk_f16_f32 v65, v66, 0
	v_mov_b32_e32 v66, 0
	v_mov_b32_e32 v67, 0
	v_cvt_pk_f16_f32 v68, v68, v69
	v_mul_f32_e32 v70, v103, v70
	v_cvt_pk_f16_f32 v69, v70, 0
	v_mov_b32_e32 v70, 0
	v_mov_b32_e32 v71, 0
	v_cvt_pk_f16_f32 v72, v72, v73
	v_mul_f32_e32 v74, v103, v74
	v_cvt_pk_f16_f32 v73, v74, 0
	v_mov_b32_e32 v74, 0
	v_mov_b32_e32 v75, 0
	v_cvt_pk_f16_f32 v76, v76, v77
	v_mul_f32_e32 v78, v103, v78
	v_cvt_pk_f16_f32 v77, v78, 0
	v_mov_b32_e32 v78, 0
	v_mov_b32_e32 v79, 0
	v_cvt_pk_f16_f32 v80, v80, v81
	v_mul_f32_e32 v82, v103, v82
	v_cvt_pk_f16_f32 v81, v82, 0
	v_mov_b32_e32 v82, 0
	v_mov_b32_e32 v83, 0
	v_cvt_pk_f16_f32 v84, v84, v85
	v_mul_f32_e32 v86, v103, v86
	v_cvt_pk_f16_f32 v85, v86, 0
	v_mov_b32_e32 v86, 0
	v_mov_b32_e32 v87, 0
	v_cvt_pk_f16_f32 v88, v88, v89
	v_mul_f32_e32 v90, v103, v90
	v_cvt_pk_f16_f32 v89, v90, 0
	v_mov_b32_e32 v90, 0
	v_mov_b32_e32 v91, 0
	v_cvt_pk_f16_f32 v92, v92, v93
	v_mul_f32_e32 v94, v103, v94
	v_cvt_pk_f16_f32 v93, v94, 0
	v_mov_b32_e32 v94, 0
	v_mov_b32_e32 v95, 0
	v_mov_b32_e32 v34, 0
	v_mov_b32_e32 v35, 0
	v_mov_b32_e32 v40, 0
	v_mov_b32_e32 v41, 0
	v_add_u32_e32 v14, 3, v96
	v_lshrrev_b32_e32 v14, 2, v14
	v_add_u32_e32 v15, v97, v14
	v_add_u32_e32 v16, v97, v99
	v_mov_b32_e32 v13, 0x1ce00
	s_mov_b64 s[58:59], exec

.Llin_skip:
	s_mov_b64 exec, s[58:59]
	s_nop 4
	v_add_f32_dpp v40, v40, v40 quad_perm:[1,0,3,2] row_mask:0xf bank_mask:0xf
	v_add_f32_dpp v41, v41, v41 quad_perm:[1,0,3,2] row_mask:0xf bank_mask:0xf
	s_nop 1
	v_add_f32_dpp v40, v40, v40 quad_perm:[2,3,0,1] row_mask:0xf bank_mask:0xf
	v_add_f32_dpp v41, v41, v41 quad_perm:[2,3,0,1] row_mask:0xf bank_mask:0xf
	v_cmp_eq_u32_e32 vcc, 0, v99
	s_movk_i32 s45, 0xe0
	v_cmp_gt_u32_e64 s[60:61], s45, v98
	v_add_u32_e32 v12, 0x38000000, v101
	v_cvt_f32_u32_e32 v48, v96
	s_and_b64 vcc, vcc, s[60:61]
	s_and_saveexec_b64 s[60:61], vcc
	v_mov_b32_e32 v49, v100
	v_mul_f32_e32 v12, v12, v20
	v_mul_f32_e32 v46, v40, v100
	v_mul_f32_e32 v47, v41, v100
	v_mul_f32_e32 v48, v48, v100
	v_lshlrev_b32_e32 v13, 4, v98
	v_add_u32_e32 v13, 0x23360, v13
	ds_write_b128 v13, v[46:49]
	v_lshlrev_b32_e32 v13, 2, v98
	v_add_u32_e32 v13, 0x22200, v13
	ds_write_b32 v13, v12
	s_mov_b64 exec, s[60:61]
	s_waitcnt lgkmcnt(0)
	s_barrier
	v_mov_b32_e32 v11, 0x24860
	ds_read_b64 v[12:13], v11
	v_mov_b32_e32 v62, 0x23360
	v_mov_b32_e32 v2, v55
	s_waitcnt lgkmcnt(0)
	v_readfirstlane_b32 s62, v12
	v_readfirstlane_b32 s63, v13
	s_add_i32 s62, s62, 1
	s_lshr_b32 s62, s62, 1
	s_add_i32 s63, s63, 1
	s_lshr_b32 s63, s63, 1
